# V tile by LDS-DMA in both attention phases, early V fragment reads, later code kept at the baseline address modulo 64
# speedup vs baseline: 1.0065x; 1.0065x over previous
; __device__ __forceinline__ unsigned xb_ld(unsigned* p)              { return __hip_atomic_load(p, __ATOMIC_RELAXED, __HIP_MEMORY_SCOPE_AGENT); }
; __device__ __forceinline__ void xcd_barrier_complete(unsigned* bar, unsigned x, unsigned& nloc, unsigned& nx) {
;     const unsigned G = gridDim.x * gridDim.y * gridDim.z;
;     unsigned sum, cnt, mine, sp = 0u;
;     for (;;) {
;         sum = 0u; cnt = 0u; mine = 0u;
; #pragma unroll
;         for (unsigned j = 0; j < 16; ++j) { const unsigned c = xb_ld(&bar[XB_XCNT(j)]); sum += c; cnt += (c > 0u) ? 1u : 0u; mine = (j == x) ? c : mine; }
;         if (sum == G) break;
;         __builtin_amdgcn_s_sleep(1);
;         if ((++sp & 255u) == 0u) { if (xb_ld(&bar[XB_TMO])) break; if (sp > XB_SPIN_CAP) { atomicAdd(&bar[XB_TMO], 1u); break; } }
;     }
;     nloc = mine > 0u ? mine : 1u; nx = cnt > 0u ? cnt : 1u;
; }
; __device__ __forceinline__ void xcd_barrier(const XcdBarrier& b) {
;     asm volatile("s_waitcnt vmcnt(0)" ::: "memory");
;     __syncthreads();
;     if (threadIdx.x == 0) {
;         unsigned* bar = b.bar;
;         __builtin_amdgcn_s_waitcnt(0);
;         unsigned nloc = b.st[0], nx = b.st[1];
;         if (nloc == 0u) { xcd_barrier_complete(bar, b.x, nloc, nx); b.st[0] = nloc; b.st[1] = nx; }
.LBB0_653:
	s_nop 0
	s_nop 0
	s_nop 0
	s_nop 0
	s_nop 0
	s_nop 0
	s_nop 0
	s_nop 0
	s_nop 0
	s_nop 0
	s_cmp_gt_i32 s81, 8
	s_cselect_b64 s[4:5], -1, 0
	s_and_b64 s[0:1], s[10:11], s[4:5]
	s_andn2_b64 vcc, exec, s[0:1]
	s_cbranch_vccnz .LBB0_707
	s_mov_b64 s[8:9], s[96:97]
	s_getreg_b32 s0, hwreg(HW_REG_XCC_ID, 0, 4)
	s_waitcnt vmcnt(0)
	s_waitcnt vmcnt(0)
	s_barrier
	s_mov_b64 s[6:7], exec
	v_readlane_b32 s2, v255, 0
	v_readlane_b32 s3, v255, 1
	s_and_b64 s[2:3], s[6:7], s[2:3]
	s_mov_b64 exec, s[2:3]
	s_cbranch_execz .LBB0_706
	s_add_i32 s1, 0, 0x22160
	v_mov_b32_e32 v2, s1
	s_load_dwordx2 s[8:9], s[8:9], 0xe8
	s_waitcnt vmcnt(0) expcnt(0) lgkmcnt(0)
	ds_read_b32 v4, v2
	s_add_i32 s1, 0, 0x22164
	v_mov_b32_e32 v2, s1
	ds_read_b32 v2, v2
	s_and_b32 s0, s0, 15
	s_waitcnt lgkmcnt(1)
	v_cmp_ne_u32_e32 vcc, 0, v4
	s_cbranch_vccnz .LBB0_670
	s_add_u32 s10, s8, 0x4200
	s_addc_u32 s11, s9, 0
	s_add_u32 s12, s8, 0x4400
	s_addc_u32 s13, s9, 0
	s_add_u32 s14, s8, 0x4500
	s_addc_u32 s15, s9, 0
	s_add_u32 s16, s8, 0x4600
	s_addc_u32 s17, s9, 0
	s_add_u32 s18, s8, 0x4700
	s_addc_u32 s19, s9, 0
	s_add_u32 s20, s8, 0x4800
	s_addc_u32 s21, s9, 0
	s_add_u32 s22, s8, 0x4900
	s_addc_u32 s23, s9, 0
	s_add_u32 s24, s8, 0x4a00
	s_addc_u32 s25, s9, 0
	s_add_u32 s26, s8, 0x4b00
	s_addc_u32 s27, s9, 0
	s_add_u32 s28, s8, 0x4c00
	s_addc_u32 s29, s9, 0
	s_add_u32 s30, s8, 0x4d00
	s_addc_u32 s31, s9, 0
	s_add_u32 s34, s8, 0x4e00
	s_addc_u32 s35, s9, 0
	s_add_u32 s36, s8, 0x4f00
	s_addc_u32 s37, s9, 0
	s_add_u32 s38, s8, 0x5000
	s_addc_u32 s39, s9, 0
	s_load_dwordx2 s[2:3], s[96:97], 0xf8
	s_load_dword s1, s[96:97], 0x100
	s_add_u32 s40, s8, 0x5100
	s_addc_u32 s41, s9, 0
	s_add_u32 s42, s8, 0x5200
	s_addc_u32 s43, s9, 0
	s_waitcnt lgkmcnt(0)
	s_mul_i32 s2, s3, s2
	s_add_u32 s44, s8, 0x5300
	s_mul_i32 s1, s2, s1
	s_addc_u32 s45, s9, 0
	s_mov_b32 s2, 1
	v_mov_b32_e32 v18, 0
	s_branch .LBB0_658

; __device__ __forceinline__ unsigned xb_ld(unsigned* p)              { return __hip_atomic_load(p, __ATOMIC_RELAXED, __HIP_MEMORY_SCOPE_AGENT); }
; __device__ __forceinline__ void xcd_barrier_complete(unsigned* bar, unsigned x, unsigned& nloc, unsigned& nx) {
;     const unsigned G = gridDim.x * gridDim.y * gridDim.z;
;     unsigned sum, cnt, mine, sp = 0u;
;     for (;;) {
;         sum = 0u; cnt = 0u; mine = 0u;
; #pragma unroll
;         for (unsigned j = 0; j < 16; ++j) { const unsigned c = xb_ld(&bar[XB_XCNT(j)]); sum += c; cnt += (c > 0u) ? 1u : 0u; mine = (j == x) ? c : mine; }
;         if (sum == G) break;
;         __builtin_amdgcn_s_sleep(1);
;         if ((++sp & 255u) == 0u) { if (xb_ld(&bar[XB_TMO])) break; if (sp > XB_SPIN_CAP) { atomicAdd(&bar[XB_TMO], 1u); break; } }
;     }
;     nloc = mine > 0u ? mine : 1u; nx = cnt > 0u ? cnt : 1u;
; }
; __device__ __forceinline__ void xcd_barrier(const XcdBarrier& b) {
;     asm volatile("s_waitcnt vmcnt(0)" ::: "memory");
;     __syncthreads();
;     if (threadIdx.x == 0) {
;         unsigned* bar = b.bar;
;         __builtin_amdgcn_s_waitcnt(0);
;         unsigned nloc = b.st[0], nx = b.st[1];
;         if (nloc == 0u) { xcd_barrier_complete(bar, b.x, nloc, nx); b.st[0] = nloc; b.st[1] = nx; }
.LBB0_1284:
	s_nop 0
	s_nop 0
	s_nop 0
	s_nop 0
	s_nop 0
	s_nop 0
	s_nop 0
	s_nop 0
	s_nop 0
	s_nop 0
	s_nop 0
	s_cmp_gt_i32 s81, 16
	s_cselect_b64 s[4:5], -1, 0
	s_and_b64 s[0:1], s[24:25], s[4:5]
	s_andn2_b64 vcc, exec, s[0:1]
	s_cbranch_vccnz .LBB0_1338
	s_mov_b64 s[8:9], s[96:97]
	s_getreg_b32 s0, hwreg(HW_REG_XCC_ID, 0, 4)
	s_waitcnt vmcnt(0)
	s_waitcnt vmcnt(0) lgkmcnt(0)
	s_barrier
	s_mov_b64 s[6:7], exec
	v_readlane_b32 s2, v255, 0
	v_readlane_b32 s3, v255, 1
	s_and_b64 s[2:3], s[6:7], s[2:3]
	s_mov_b64 exec, s[2:3]
	s_cbranch_execz .LBB0_1337
	s_add_i32 s1, 0, 0x22160
	v_mov_b32_e32 v1, s1
	s_load_dwordx2 s[8:9], s[8:9], 0xe8
	s_waitcnt vmcnt(0) expcnt(0) lgkmcnt(0)
	ds_read_b32 v3, v1
	s_add_i32 s1, 0, 0x22164
	v_mov_b32_e32 v1, s1
	ds_read_b32 v1, v1
	s_and_b32 s0, s0, 15
	s_waitcnt lgkmcnt(1)
	v_cmp_ne_u32_e32 vcc, 0, v3
	s_cbranch_vccnz .LBB0_1301
	s_add_u32 s10, s8, 0x4200
	s_addc_u32 s11, s9, 0
	s_add_u32 s12, s8, 0x4400
	s_addc_u32 s13, s9, 0
	s_add_u32 s14, s8, 0x4500
	s_addc_u32 s15, s9, 0
	s_add_u32 s16, s8, 0x4600
	s_addc_u32 s17, s9, 0
	s_add_u32 s18, s8, 0x4700
	s_addc_u32 s19, s9, 0
	s_add_u32 s20, s8, 0x4800
	s_addc_u32 s21, s9, 0
	s_add_u32 s22, s8, 0x4900
	s_addc_u32 s23, s9, 0
	s_add_u32 s24, s8, 0x4a00
	s_addc_u32 s25, s9, 0
	s_add_u32 s26, s8, 0x4b00
	s_addc_u32 s27, s9, 0
	s_add_u32 s28, s8, 0x4c00
	s_addc_u32 s29, s9, 0
	s_add_u32 s30, s8, 0x4d00
	s_addc_u32 s31, s9, 0
	s_add_u32 s34, s8, 0x4e00
	s_addc_u32 s35, s9, 0
	s_add_u32 s36, s8, 0x4f00
	s_addc_u32 s37, s9, 0
	s_add_u32 s38, s8, 0x5000
	s_addc_u32 s39, s9, 0
	s_load_dwordx2 s[2:3], s[96:97], 0xf8
	s_load_dword s1, s[96:97], 0x100
	s_add_u32 s40, s8, 0x5100
	s_addc_u32 s41, s9, 0
	s_add_u32 s42, s8, 0x5200
	s_addc_u32 s43, s9, 0
	s_waitcnt lgkmcnt(0)
	s_mul_i32 s2, s3, s2
	s_add_u32 s44, s8, 0x5300
	s_mul_i32 s1, s2, s1
	s_addc_u32 s45, s9, 0
	s_mov_b32 s2, 1
	v_mov_b32_e32 v17, 0
	s_branch .LBB0_1289
